# speedup vs baseline: 1.0772x; 1.0772x over previous
_Z11knrm_kernelPKfS0_PKiS2_S0_Pf:
	v_lshrrev_b32_e32 v1, 6, v0
	s_load_dwordx8 s[4:11], s[0:1], 0x0
	s_load_dwordx4 s[12:15], s[0:1], 0x20
	v_lshlrev_b32_e32 v2, 2, v0
	v_bfe_u32 v3, v0, 2, 2
	v_lshlrev_b32_e32 v124, 5, v1
	v_and_or_b32 v98, v2, 12, v3
	v_lshl_or_b32 v8, s2, 8, v124
	v_or_b32_e32 v2, v8, v98
	v_ashrrev_i32_e32 v3, 31, v2
	s_waitcnt lgkmcnt(0)
	v_lshl_add_u64 v[4:5], v[2:3], 2, s[10:11]
	v_or_b32_e32 v2, 24, v2
	v_and_or_b32 v6, v98, 7, v8
	v_ashrrev_i32_e32 v3, 31, v2
	s_movk_i32 s0, 0x160
	v_ashrrev_i32_e32 v7, 31, v6
	v_lshl_add_u64 v[2:3], v[2:3], 2, s[10:11]
	v_lshrrev_b32_e32 v121, 5, v0
	v_cmp_gt_u32_e64 s[0:1], s0, v0
	v_lshl_add_u64 v[6:7], v[6:7], 2, s[10:11]
	global_load_dword v125, v[6:7], off
	global_load_dword v126, v[6:7], off offset:64
	global_load_dword v127, v[6:7], off offset:96
	global_load_dword v190, v[6:7], off offset:32
	v_cndmask_b32_e64 v2, 10, v121, s[0:1]
	v_lshlrev_b32_e32 v2, 2, v2
	s_lshl_b32 s3, s2, 5
	v_and_b32_e32 v122, 31, v0
	global_load_dword v118, v2, s[12:13]
	v_or_b32_e32 v2, s3, v122
	v_ashrrev_i32_e32 v3, 31, v2
	v_lshl_add_u64 v[2:3], v[2:3], 2, s[8:9]
	v_lshrrev_b32_e32 v100, 4, v0
	global_load_dword v119, v[2:3], off
	v_or_b32_e32 v2, s3, v100
	s_movk_i32 s3, 0x4b0
	v_and_b32_e32 v123, 15, v0
	s_mov_b32 s19, 0x20000
	v_mul_lo_u32 v2, v2, s3
	v_and_b32_e32 v120, 63, v0
	s_mov_b64 s[16:17], s[6:7]
	s_and_b32 s5, s5, 0xffff
	s_mov_b32 s6, 0x960000
	s_mov_b32 s7, s19
	v_lshl_add_u32 v3, v123, 4, v2
	v_mul_lo_u32 v99, v8, s3
	v_lshlrev_b32_e32 v132, 4, v120
	buffer_load_dwordx4 v[90:93], v3, s[4:7], 0 offen nt
	buffer_load_dwordx4 v[86:89], v3, s[4:7], 0 offen offset:256 nt
	buffer_load_dwordx4 v[82:85], v3, s[4:7], 0 offen offset:512 nt
	buffer_load_dwordx4 v[78:81], v3, s[4:7], 0 offen offset:768 nt
	v_min_u32_e32 v3, 10, v123
	v_add_u32_e32 v192, v99, v132
	s_mov_b32 s18, 0x4b00000
	s_and_b32 s17, s17, 0xffff
	v_lshl_add_u32 v2, v3, 4, v2
	v_min_u32_e32 v193, 23, v120
	s_movk_i32 s27, 0x1000
	s_movk_i32 s28, 0x2000
	v_lshlrev_b32_e32 v193, 4, v193
	buffer_load_dwordx4 v[94:97], v2, s[4:7], 0 offen offset:1024 nt
	v_add3_u32 v193, v99, v193, s28
	buffer_load_dwordx4 v[2:5], v192, s[16:19], 0 offen nt
	buffer_load_dwordx4 v[14:17], v192, s[16:19], 0 offen offset:1024 nt
	buffer_load_dwordx4 v[34:37], v192, s[16:19], 0 offen offset:2048 nt
	buffer_load_dwordx4 v[46:49], v192, s[16:19], 0 offen offset:3072 nt
	buffer_load_dwordx4 v[54:57], v192, s[16:19], s27 offen nt
	buffer_load_dwordx4 v[58:61], v192, s[16:19], s27 offen offset:1024 nt
	buffer_load_dwordx4 v[62:65], v192, s[16:19], s27 offen offset:2048 nt
	buffer_load_dwordx4 v[66:69], v192, s[16:19], s27 offen offset:3072 nt
	buffer_load_dwordx4 v[70:73], v192, s[16:19], s28 offen nt
	buffer_load_dwordx4 v[74:77], v193, s[16:19], 0 offen offset:1024 nt
	s_mov_b32 s3, 0
	v_mul_u32_u24_e32 v131, 0x2600, v1
	v_cmp_gt_u32_e64 s[4:5], 16, v120
	s_and_saveexec_b64 s[6:7], s[4:5]
	s_movk_i32 s8, 0x260
	v_mov_b32_e32 v102, 0
	v_mad_u32_u24 v101, v120, s8, v131
	v_mov_b32_e32 v103, v102
	ds_write_b64 v101, v[102:103] offset:20056
	s_or_b64 exec, exec, s[6:7]
	v_cmp_lt_u32_e32 vcc, 10, v123
	s_waitcnt vmcnt(13)
	v_mul_f32_e32 v101, v87, v87
	v_mov_b32_e32 v106, v92
	s_waitcnt vmcnt(10)
	v_cndmask_b32_e64 v103, v97, 0, vcc
	v_cndmask_b32_e64 v102, v96, 0, vcc
	v_mov_b32_e32 v96, v91
	v_mov_b32_e32 v97, v83
	v_cndmask_b32_e64 v105, v95, 0, vcc
	v_cndmask_b32_e64 v104, v94, 0, vcc
	v_mov_b32_e32 v94, v90
	v_mov_b32_e32 v95, v82
	v_pk_mul_f32 v[96:97], v[96:97], v[96:97]
	v_mov_b32_e32 v107, v84
	v_fmac_f32_e32 v101, v86, v86
	v_pk_fma_f32 v[94:95], v[94:95], v[94:95], v[96:97]
	v_mov_b32_e32 v108, v93
	v_mov_b32_e32 v109, v85
	v_fmac_f32_e32 v101, v88, v88
	v_pk_fma_f32 v[94:95], v[106:107], v[106:107], v[94:95]
	v_fmac_f32_e32 v101, v89, v89
	v_pk_fma_f32 v[94:95], v[108:109], v[108:109], v[94:95]
	v_mov_b32_e32 v96, v79
	v_add_f32_e32 v94, v94, v101
	v_mov_b32_e32 v97, v105
	v_add_f32_e32 v101, v94, v95
	v_mov_b32_e32 v94, v78
	v_mov_b32_e32 v95, v104
	v_pk_mul_f32 v[96:97], v[96:97], v[96:97]
	s_mov_b32 s21, 0xf800000
	v_pk_fma_f32 v[94:95], v[94:95], v[94:95], v[96:97]
	v_mov_b32_e32 v96, v80
	v_mov_b32_e32 v97, v102
	v_pk_fma_f32 v[94:95], v[96:97], v[96:97], v[94:95]
	v_mov_b32_e32 v96, v81
	v_mov_b32_e32 v97, v103
	v_pk_fma_f32 v[94:95], v[96:97], v[96:97], v[94:95]
	v_mov_b32_e32 v135, 0x260
	v_add_f32_e32 v94, v101, v94
	v_add_f32_e32 v94, v94, v95
	v_mbcnt_lo_u32_b32 v95, -1, 0
	v_mbcnt_hi_u32_b32 v95, -1, v95
	v_and_b32_e32 v97, 64, v95
	v_xor_b32_e32 v96, 1, v95
	v_add_u32_e32 v101, 64, v97
	v_cmp_lt_i32_e32 vcc, v96, v101
	s_movk_i32 s8, 0x260
	v_add_u32_e32 v137, 0x4b00, v99
	v_cndmask_b32_e32 v96, v95, v96, vcc
	v_lshlrev_b32_e32 v97, 2, v96
	ds_bpermute_b32 v96, v97, v94
	s_movk_i32 s10, 0x1b5
	v_mov_b32_e32 v99, 0x36a00
	v_mov_b32_e32 v111, 0x666c0
	v_mov_b32_e32 v113, 0x6d400
	s_waitcnt lgkmcnt(0)
	v_add_f32_e32 v94, v94, v96
	v_xor_b32_e32 v96, 2, v95
	v_cmp_lt_i32_e32 vcc, v96, v101
	v_mov_b32_e32 v115, 0x74140
	s_mov_b32 s20, 0xbeb17218
	v_cndmask_b32_e32 v96, v95, v96, vcc
	v_lshlrev_b32_e32 v128, 2, v96
	ds_bpermute_b32 v96, v128, v94
	s_mov_b32 s22, 0x44132d1f
	v_mov_b32_e32 v161, 0xc47a0000
	s_waitcnt lgkmcnt(0)
	v_add_f32_e32 v94, v94, v96
	v_xor_b32_e32 v96, 4, v95
	v_cmp_lt_i32_e32 vcc, v96, v101
	s_nop 1
	v_cndmask_b32_e32 v96, v95, v96, vcc
	v_lshlrev_b32_e32 v129, 2, v96
	ds_bpermute_b32 v96, v129, v94
	s_waitcnt lgkmcnt(0)
	v_add_f32_e32 v94, v94, v96
	v_xor_b32_e32 v96, 8, v95
	v_cmp_lt_i32_e32 vcc, v96, v101
	s_nop 1
	v_cndmask_b32_e32 v96, v95, v96, vcc
	v_lshlrev_b32_e32 v130, 2, v96
	ds_bpermute_b32 v96, v130, v94
	s_waitcnt lgkmcnt(0)
	v_add_f32_e32 v94, v94, v96
	v_mul_f32_e32 v96, 0x4f800000, v94
	v_cmp_gt_f32_e32 vcc, s21, v94
	s_nop 1
	v_cndmask_b32_e32 v94, v94, v96, vcc
	v_sqrt_f32_e32 v96, v94
	s_nop 0
	v_add_u32_e32 v106, -1, v96
	v_fma_f32 v107, -v106, v96, v94
	v_cmp_ge_f32_e64 s[6:7], 0, v107
	v_add_u32_e32 v107, 1, v96
	s_nop 0
	v_cndmask_b32_e64 v106, v96, v106, s[6:7]
	v_fma_f32 v96, -v107, v96, v94
	v_cmp_lt_f32_e64 s[6:7], 0, v96
	s_nop 1
	v_cndmask_b32_e64 v96, v106, v107, s[6:7]
	v_mul_f32_e32 v106, 0x37800000, v96
	v_cndmask_b32_e32 v96, v96, v106, vcc
	v_cmp_class_f32_e32 vcc, v94, v135
	s_nop 1
	v_cndmask_b32_e32 v94, v96, v94, vcc
	v_add_f32_e32 v96, 0x29e12e13, v94
	v_div_scale_f32 v106, s[6:7], v96, v96, 1.0
	v_rcp_f32_e32 v107, v106
	v_mov_b32_e32 v94, 0
	v_cmp_gt_u32_e64 s[6:7], 48, v120
	v_mov_b32_e32 v116, v94
	v_fma_f32 v108, -v106, v107, 1.0
	v_fmac_f32_e32 v107, v108, v107
	v_div_scale_f32 v108, vcc, 1.0, v96, 1.0
	v_mul_f32_e32 v109, v108, v107
	v_fma_f32 v110, -v106, v109, v108
	v_fmac_f32_e32 v109, v110, v107
	v_fma_f32 v106, -v106, v109, v108
	v_div_fmas_f32 v106, v106, v107, v109
	v_div_fixup_f32 v96, v106, v96, 1.0
	v_lshlrev_b32_e32 v106, 3, v123
	v_pk_mul_f32 v[82:83], v[96:97], v[82:83] op_sel_hi:[0,1]
	v_pk_mul_f32 v[84:85], v[96:97], v[84:85] op_sel_hi:[0,1]
	v_pk_mul_f32 v[78:79], v[96:97], v[78:79] op_sel_hi:[0,1]
	v_pk_mul_f32 v[80:81], v[96:97], v[80:81] op_sel_hi:[0,1]
	v_mad_u32_u24 v100, v100, s8, v106
	v_cvt_pk_f16_f32 v82, v82, v83
	v_cvt_pk_f16_f32 v83, v84, v85
	v_cvt_pk_f16_f32 v78, v78, v79
	v_cvt_pk_f16_f32 v79, v80, v81
	ds_write2_b64 v100, v[82:83], v[78:79] offset0:32 offset1:48
	v_min_u32_e32 v82, 23, v120
	v_mov_b32_e32 v83, 0x2400
	v_lshl_or_b32 v138, v82, 4, v83
	v_xor_b32_e32 v83, 16, v95
	v_cmp_lt_i32_e32 vcc, v83, v101
	v_pk_mul_f32 v[90:91], v[96:97], v[90:91] op_sel_hi:[0,1]
	v_pk_mul_f32 v[92:93], v[96:97], v[92:93] op_sel_hi:[0,1]
	v_cndmask_b32_e32 v83, v95, v83, vcc
	v_lshlrev_b32_e32 v133, 2, v83
	v_xor_b32_e32 v83, 32, v95
	v_pk_mul_f32 v[86:87], v[96:97], v[86:87] op_sel_hi:[0,1]
	v_pk_mul_f32 v[88:89], v[96:97], v[88:89] op_sel_hi:[0,1]
	v_pk_mul_f32 v[78:79], v[96:97], v[104:105] op_sel_hi:[0,1]
	v_pk_mul_f32 v[80:81], v[96:97], v[102:103] op_sel_hi:[0,1]
	v_cmp_lt_i32_e32 vcc, v83, v101
	v_cvt_pk_f16_f32 v90, v90, v91
	v_cvt_pk_f16_f32 v91, v92, v93
	v_cvt_pk_f16_f32 v86, v86, v87
	v_cvt_pk_f16_f32 v87, v88, v89
	v_cvt_pk_f16_f32 v78, v78, v79
	v_cvt_pk_f16_f32 v79, v80, v81
	v_mov_b32_e32 v81, 0x17c00
	v_cndmask_b32_e32 v83, v95, v83, vcc
	ds_write2_b64 v100, v[90:91], v[86:87] offset1:16
	v_sub_u32_e64 v80, v123, 11 clamp
	v_lshl_or_b32 v81, v1, 7, v81
	v_lshlrev_b32_e32 v134, 2, v83
	v_or_b32_e32 v83, 64, v120
	v_mov_b32_e32 v86, 0x6d40
	v_mov_b32_e32 v87, 0xda80
	v_mov_b32_e32 v89, 0x147c0
	v_mov_b32_e32 v91, 0x1b500
	v_mov_b32_e32 v93, 0x28f80
	v_mov_b32_e32 v96, 0x2fcc0
	v_mov_b32_e32 v101, 0x3d740
	v_mov_b32_e32 v103, 0x44480
	v_mov_b32_e32 v105, 0x4b1c0
	v_mov_b32_e32 v107, 0x58c40
	v_or_b32_e32 v109, 0x3c0, v0
	v_mad_i32_i24 v80, v80, -8, v100
	v_lshrrev_b32_e32 v82, 1, v120
	v_lshl_add_u32 v139, v120, 2, v81
	v_and_or_b32 v140, v120, 48, v81
	v_lshlrev_b32_e32 v81, 3, v120
	v_mul_u32_u24_e32 v84, 0x1b5, v83
	v_lshl_add_u32 v85, v83, 3, v131
	v_mad_u32_u24 v86, v83, s10, v86
	v_mad_u32_u24 v87, v83, s10, v87
	v_mad_u32_u24 v89, v83, s10, v89
	v_mad_u32_u24 v91, v83, s10, v91
	v_mad_u32_u24 v93, v83, s10, v93
	v_mad_u32_u24 v96, v83, s10, v96
	v_mad_u32_u24 v99, v83, s10, v99
	v_mad_u32_u24 v101, v83, s10, v101
	v_mad_u32_u24 v103, v83, s10, v103
	v_mad_u32_u24 v105, v83, s10, v105
	v_mad_u32_u24 v107, v83, s10, v107
	v_mul_u32_u24_e32 v110, 0x1b5, v109
	v_mad_u32_u24 v111, v83, s10, v111
	v_mad_u32_u24 v113, v83, s10, v113
	v_mad_u32_u24 v83, v83, s10, v115
	ds_write_b64 v80, v[78:79] offset:512
	v_mul_u32_u24_e32 v78, 0x260, v123
	v_and_b32_e32 v82, 24, v82
	v_lshrrev_b32_e32 v84, 12, v84
	v_add_u32_e32 v141, v131, v81
	v_lshrrev_b32_e32 v86, 12, v86
	v_lshrrev_b32_e32 v87, 12, v87
	v_lshrrev_b32_e32 v89, 12, v89
	v_lshrrev_b32_e32 v91, 12, v91
	v_lshrrev_b32_e32 v93, 12, v93
	v_lshrrev_b32_e32 v96, 12, v96
	v_lshrrev_b32_e32 v99, 12, v99
	v_lshrrev_b32_e32 v101, 12, v101
	v_lshrrev_b32_e32 v103, 12, v103
	v_lshrrev_b32_e32 v105, 12, v105
	v_lshrrev_b32_e32 v107, 12, v107
	v_lshrrev_b32_e32 v110, 12, v110
	v_lshrrev_b32_e32 v111, 12, v111
	v_lshrrev_b32_e32 v113, 12, v113
	v_lshrrev_b32_e32 v83, 12, v83
	v_and_b32_e32 v79, 48, v0
	v_mad_u32_u24 v80, v98, s8, v131
	v_and_b32_e32 v84, 8, v84
	v_add_u32_e32 v81, 0x400, v141
	v_and_b32_e32 v86, 24, v86
	v_add_u32_e32 v88, 0x600, v141
	v_and_b32_e32 v87, 24, v87
	v_add_u32_e32 v90, 0x800, v141
	v_and_b32_e32 v89, 56, v89
	v_add_u32_e32 v92, 0xa00, v141
	v_and_b32_e32 v91, 56, v91
	v_add_u32_e32 v95, 0xe00, v141
	v_and_b32_e32 v93, 56, v93
	v_add_u32_e32 v98, 0x1000, v141
	v_and_b32_e32 v96, 56, v96
	v_add_u32_e32 v100, 0x1200, v141
	v_and_b32_e32 v99, 0x78, v99
	v_add_u32_e32 v102, 0x1400, v141
	v_and_b32_e32 v101, 0x78, v101
	v_add_u32_e32 v104, 0x1600, v141
	v_and_b32_e32 v103, 0x58, v103
	v_add_u32_e32 v106, 0x1800, v141
	v_and_b32_e32 v105, 0x58, v105
	v_add_u32_e32 v108, 0x1c00, v141
	v_and_b32_e32 v107, 0x78, v107
	v_lshl_add_u32 v109, v109, 3, v131
	v_and_b32_e32 v110, 0x78, v110
	v_add_u32_e32 v112, 0x2000, v141
	v_and_b32_e32 v111, 0x78, v111
	v_add_u32_e32 v114, 0x2200, v141
	v_and_b32_e32 v113, 0x78, v113
	v_add_u32_e32 v115, 0x2400, v141
	v_and_b32_e32 v83, 0xf8, v83
	s_movk_i32 s10, 0x4c00
	v_add_u32_e32 v78, v78, v82
	v_mad_u32_u24 v136, v123, s8, v79
	v_cmp_gt_u32_e64 s[8:9], 24, v120
	v_add3_u32 v142, v80, v79, s10
	v_add_u32_e32 v143, v85, v84
	v_add_u32_e32 v144, v81, v86
	v_add_u32_e32 v145, v88, v87
	v_add_u32_e32 v146, v90, v89
	v_add_u32_e32 v147, v92, v91
	v_add_u32_e32 v148, v95, v93
	v_add_u32_e32 v149, v98, v96
	v_add_u32_e32 v150, v100, v99
	v_add_u32_e32 v151, v102, v101
	v_add_u32_e32 v152, v104, v103
	v_add_u32_e32 v153, v106, v105
	v_add_u32_e32 v154, v108, v107
	v_add_u32_e32 v155, v109, v110
	v_add_u32_e32 v156, v112, v111
	v_add_u32_e32 v157, v114, v113
	v_add_u32_e32 v158, v115, v83
	v_add_u32_e32 v159, v80, v82
	v_add_u32_e32 v160, 64, v78
	v_mov_b32_e32 v96, 0xc604b4df
	v_mov_b32_e32 v95, v94
	v_mov_b32_e32 v98, v94
	v_mov_b32_e32 v99, v94
	v_mov_b32_e32 v100, v94
	v_mov_b32_e32 v101, v94
	v_mov_b32_e32 v102, v94
	v_mov_b32_e32 v103, v94
	v_mov_b32_e32 v104, v94
	v_mov_b32_e32 v105, v94
	v_mov_b32_e32 v106, v94
	v_mov_b32_e32 v107, v94
	v_mov_b32_e32 v108, v94
	v_mov_b32_e32 v109, v94
	v_mov_b32_e32 v110, v94
	v_mov_b32_e32 v111, v94
	v_mov_b32_e32 v112, v94
	v_mov_b32_e32 v113, v94
	v_mov_b32_e32 v114, v94
	v_mov_b32_e32 v115, v94
	v_mov_b32_e32 v117, v94
	v_cmp_lt_i32_e64 s[30:31], 1, v125
	v_cmp_lt_i32_e64 s[32:33], 1, v190
	v_cmp_lt_i32_e64 s[34:35], 1, v126
	v_cmp_lt_i32_e64 s[36:37], 1, v127
	v_cndmask_b32_e64 v191, 0, 1, s[30:31]
	v_cndmask_b32_e64 v190, 0, 2, s[32:33]
	v_cndmask_b32_e64 v126, 0, 4, s[34:35]
	v_cndmask_b32_e64 v127, 0, 8, s[36:37]
	v_or3_b32 v191, v191, v190, v126
	v_or_b32_e32 v191, v191, v127
	s_waitcnt lgkmcnt(0)
	s_barrier
	s_mov_b32 s26, 0x2580
	s_mov_b32 s27, 0x3580
	s_mov_b32 s28, 0x4580
	buffer_load_dwordx4 v[6:9], v192, s[16:19], s26 offen nt
	buffer_load_dwordx4 v[10:13], v192, s[16:19], s26 offen offset:1024 nt
	buffer_load_dwordx4 v[18:21], v192, s[16:19], s26 offen offset:2048 nt
	buffer_load_dwordx4 v[22:25], v192, s[16:19], s26 offen offset:3072 nt
	buffer_load_dwordx4 v[26:29], v192, s[16:19], s27 offen nt
	buffer_load_dwordx4 v[30:33], v192, s[16:19], s27 offen offset:1024 nt
	buffer_load_dwordx4 v[38:41], v192, s[16:19], s27 offen offset:2048 nt
	buffer_load_dwordx4 v[42:45], v192, s[16:19], s27 offen offset:3072 nt
	buffer_load_dwordx4 v[50:53], v192, s[16:19], s28 offen nt
	buffer_load_dwordx4 v[186:189], v193, s[16:19], s26 offen offset:1024 nt
	s_waitcnt vmcnt(19)
	v_cvt_pk_f16_f32 v79, v4, v5
	v_cvt_pk_f16_f32 v78, v2, v3
	ds_write_b64 v141, v[78:79] offset:19456
	s_waitcnt vmcnt(18)
	v_cvt_pk_f16_f32 v79, v16, v17
	v_cvt_pk_f16_f32 v78, v14, v15
	ds_write_b64 v143, v[78:79] offset:19456
	s_waitcnt vmcnt(17)
	v_cvt_pk_f16_f32 v79, v36, v37
	v_cvt_pk_f16_f32 v78, v34, v35
	ds_write_b64 v144, v[78:79] offset:19456
	s_waitcnt vmcnt(16)
	v_cvt_pk_f16_f32 v79, v48, v49
	v_cvt_pk_f16_f32 v78, v46, v47
	ds_write_b64 v145, v[78:79] offset:19456
	s_waitcnt vmcnt(15)
	v_cvt_pk_f16_f32 v79, v56, v57
	v_cvt_pk_f16_f32 v78, v54, v55
	ds_write_b64 v146, v[78:79] offset:19456
	s_waitcnt vmcnt(14)
	v_cvt_pk_f16_f32 v79, v60, v61
	v_cvt_pk_f16_f32 v78, v58, v59
	ds_write_b64 v147, v[78:79] offset:19456
	s_waitcnt vmcnt(13)
	v_cvt_pk_f16_f32 v79, v64, v65
	v_cvt_pk_f16_f32 v78, v62, v63
	ds_write_b64 v141, v[78:79] offset:22568
	s_waitcnt vmcnt(12)
	v_cvt_pk_f16_f32 v79, v68, v69
	v_cvt_pk_f16_f32 v78, v66, v67
	ds_write_b64 v148, v[78:79] offset:19456
	s_waitcnt vmcnt(11)
	v_cvt_pk_f16_f32 v79, v72, v73
	v_cvt_pk_f16_f32 v78, v70, v71
	ds_write_b64 v149, v[78:79] offset:19456
	s_waitcnt vmcnt(10)
	v_cvt_pk_f16_f32 v79, v76, v77
	v_cvt_pk_f16_f32 v78, v74, v75
	s_and_saveexec_b64 s[12:13], s[8:9]
	ds_write_b64 v150, v[78:79] offset:19456
	s_or_b64 exec, exec, s[12:13]
	s_mov_b32 s26, 0x4b00
	s_mov_b32 s27, 0x5b00
	s_mov_b32 s28, 0x6b00
	buffer_load_dwordx4 v[2:5], v192, s[16:19], s26 offen nt
	buffer_load_dwordx4 v[14:17], v192, s[16:19], s26 offen offset:1024 nt
	buffer_load_dwordx4 v[34:37], v192, s[16:19], s26 offen offset:2048 nt
	buffer_load_dwordx4 v[46:49], v192, s[16:19], s26 offen offset:3072 nt
	buffer_load_dwordx4 v[54:57], v192, s[16:19], s27 offen nt
	buffer_load_dwordx4 v[58:61], v192, s[16:19], s27 offen offset:1024 nt
	buffer_load_dwordx4 v[62:65], v192, s[16:19], s27 offen offset:2048 nt
	buffer_load_dwordx4 v[66:69], v192, s[16:19], s27 offen offset:3072 nt
	buffer_load_dwordx4 v[70:73], v192, s[16:19], s28 offen nt
	buffer_load_dwordx4 v[74:77], v193, s[16:19], s26 offen offset:1024 nt
	s_mov_b32 s3, 0
	s_branch .LBB0_7
.Lret0:
	s_waitcnt vmcnt(19)
	v_cvt_pk_f16_f32 v79, v8, v9
	v_cvt_pk_f16_f32 v78, v6, v7
	ds_write_b64 v141, v[78:79] offset:19456
	s_waitcnt vmcnt(18)
	v_cvt_pk_f16_f32 v79, v12, v13
	v_cvt_pk_f16_f32 v78, v10, v11
	ds_write_b64 v143, v[78:79] offset:19456
	s_waitcnt vmcnt(17)
	v_cvt_pk_f16_f32 v79, v20, v21
	v_cvt_pk_f16_f32 v78, v18, v19
	ds_write_b64 v144, v[78:79] offset:19456
	s_waitcnt vmcnt(16)
	v_cvt_pk_f16_f32 v79, v24, v25
	v_cvt_pk_f16_f32 v78, v22, v23
	ds_write_b64 v145, v[78:79] offset:19456
	s_waitcnt vmcnt(15)
	v_cvt_pk_f16_f32 v79, v28, v29
	v_cvt_pk_f16_f32 v78, v26, v27
	ds_write_b64 v146, v[78:79] offset:19456
	s_waitcnt vmcnt(14)
	v_cvt_pk_f16_f32 v79, v32, v33
	v_cvt_pk_f16_f32 v78, v30, v31
	ds_write_b64 v147, v[78:79] offset:19456
	s_waitcnt vmcnt(13)
	v_cvt_pk_f16_f32 v79, v40, v41
	v_cvt_pk_f16_f32 v78, v38, v39
	ds_write_b64 v141, v[78:79] offset:22568
	s_waitcnt vmcnt(12)
	v_cvt_pk_f16_f32 v79, v44, v45
	v_cvt_pk_f16_f32 v78, v42, v43
	ds_write_b64 v148, v[78:79] offset:19456
	s_waitcnt vmcnt(11)
	v_cvt_pk_f16_f32 v79, v52, v53
	v_cvt_pk_f16_f32 v78, v50, v51
	ds_write_b64 v149, v[78:79] offset:19456
	s_waitcnt vmcnt(10)
	v_cvt_pk_f16_f32 v79, v188, v189
	v_cvt_pk_f16_f32 v78, v186, v187
	s_and_saveexec_b64 s[12:13], s[8:9]
	ds_write_b64 v150, v[78:79] offset:19456
	s_or_b64 exec, exec, s[12:13]
	s_mov_b32 s26, 0x7080
	s_mov_b32 s27, 0x8080
	s_mov_b32 s28, 0x9080
	buffer_load_dwordx4 v[6:9], v192, s[16:19], s26 offen nt
	buffer_load_dwordx4 v[10:13], v192, s[16:19], s26 offen offset:1024 nt
	buffer_load_dwordx4 v[18:21], v192, s[16:19], s26 offen offset:2048 nt
	buffer_load_dwordx4 v[22:25], v192, s[16:19], s26 offen offset:3072 nt
	buffer_load_dwordx4 v[26:29], v192, s[16:19], s27 offen nt
	buffer_load_dwordx4 v[30:33], v192, s[16:19], s27 offen offset:1024 nt
	buffer_load_dwordx4 v[38:41], v192, s[16:19], s27 offen offset:2048 nt
	buffer_load_dwordx4 v[42:45], v192, s[16:19], s27 offen offset:3072 nt
	buffer_load_dwordx4 v[50:53], v192, s[16:19], s28 offen nt
	buffer_load_dwordx4 v[186:189], v193, s[16:19], s26 offen offset:1024 nt
	s_mov_b32 s3, 1
	s_branch .LBB0_7
.Lret1:
	s_waitcnt vmcnt(19)
	v_cvt_pk_f16_f32 v79, v4, v5
	v_cvt_pk_f16_f32 v78, v2, v3
	ds_write_b64 v141, v[78:79] offset:19456
	s_waitcnt vmcnt(18)
	v_cvt_pk_f16_f32 v79, v16, v17
	v_cvt_pk_f16_f32 v78, v14, v15
	ds_write_b64 v143, v[78:79] offset:19456
	s_waitcnt vmcnt(17)
	v_cvt_pk_f16_f32 v79, v36, v37
	v_cvt_pk_f16_f32 v78, v34, v35
	ds_write_b64 v144, v[78:79] offset:19456
	s_waitcnt vmcnt(16)
	v_cvt_pk_f16_f32 v79, v48, v49
	v_cvt_pk_f16_f32 v78, v46, v47
	ds_write_b64 v145, v[78:79] offset:19456
	s_waitcnt vmcnt(15)
	v_cvt_pk_f16_f32 v79, v56, v57
	v_cvt_pk_f16_f32 v78, v54, v55
	ds_write_b64 v146, v[78:79] offset:19456
	s_waitcnt vmcnt(14)
	v_cvt_pk_f16_f32 v79, v60, v61
	v_cvt_pk_f16_f32 v78, v58, v59
	ds_write_b64 v147, v[78:79] offset:19456
	s_waitcnt vmcnt(13)
	v_cvt_pk_f16_f32 v79, v64, v65
	v_cvt_pk_f16_f32 v78, v62, v63
	ds_write_b64 v141, v[78:79] offset:22568
	s_waitcnt vmcnt(12)
	v_cvt_pk_f16_f32 v79, v68, v69
	v_cvt_pk_f16_f32 v78, v66, v67
	ds_write_b64 v148, v[78:79] offset:19456
	s_waitcnt vmcnt(11)
	v_cvt_pk_f16_f32 v79, v72, v73
	v_cvt_pk_f16_f32 v78, v70, v71
	ds_write_b64 v149, v[78:79] offset:19456
	s_waitcnt vmcnt(10)
	v_cvt_pk_f16_f32 v79, v76, v77
	v_cvt_pk_f16_f32 v78, v74, v75
	s_and_saveexec_b64 s[12:13], s[8:9]
	ds_write_b64 v150, v[78:79] offset:19456
	s_or_b64 exec, exec, s[12:13]
	s_mov_b32 s3, 2
	s_branch .LBB0_7
.Lret2:
	s_waitcnt vmcnt(9)
	v_cvt_pk_f16_f32 v79, v8, v9
	v_cvt_pk_f16_f32 v78, v6, v7
	ds_write_b64 v141, v[78:79] offset:19456
	s_waitcnt vmcnt(8)
	v_cvt_pk_f16_f32 v79, v12, v13
	v_cvt_pk_f16_f32 v78, v10, v11
	ds_write_b64 v143, v[78:79] offset:19456
	s_waitcnt vmcnt(7)
	v_cvt_pk_f16_f32 v79, v20, v21
	v_cvt_pk_f16_f32 v78, v18, v19
	ds_write_b64 v144, v[78:79] offset:19456
	s_waitcnt vmcnt(6)
	v_cvt_pk_f16_f32 v79, v24, v25
	v_cvt_pk_f16_f32 v78, v22, v23
	ds_write_b64 v145, v[78:79] offset:19456
	s_waitcnt vmcnt(5)
	v_cvt_pk_f16_f32 v79, v28, v29
	v_cvt_pk_f16_f32 v78, v26, v27
	ds_write_b64 v146, v[78:79] offset:19456
	s_waitcnt vmcnt(4)
	v_cvt_pk_f16_f32 v79, v32, v33
	v_cvt_pk_f16_f32 v78, v30, v31
	ds_write_b64 v147, v[78:79] offset:19456
	s_waitcnt vmcnt(3)
	v_cvt_pk_f16_f32 v79, v40, v41
	v_cvt_pk_f16_f32 v78, v38, v39
	ds_write_b64 v141, v[78:79] offset:22568
	s_waitcnt vmcnt(2)
	v_cvt_pk_f16_f32 v79, v44, v45
	v_cvt_pk_f16_f32 v78, v42, v43
	ds_write_b64 v148, v[78:79] offset:19456
	s_waitcnt vmcnt(1)
	v_cvt_pk_f16_f32 v79, v52, v53
	v_cvt_pk_f16_f32 v78, v50, v51
	ds_write_b64 v149, v[78:79] offset:19456
	s_waitcnt vmcnt(0)
	v_cvt_pk_f16_f32 v79, v188, v189
	v_cvt_pk_f16_f32 v78, v186, v187
	s_and_saveexec_b64 s[12:13], s[8:9]
	ds_write_b64 v150, v[78:79] offset:19456
	s_or_b64 exec, exec, s[12:13]
	s_mov_b32 s3, 3
.LBB0_7:
	v_mov_b32_e32 v86, 0
	v_mov_b32_e32 v78, 0
	v_mov_b32_e32 v79, 0
	v_mov_b32_e32 v80, 0
	v_mov_b32_e32 v81, 0
	v_mov_b32_e32 v82, 0
	v_mov_b32_e32 v83, 0
	v_mov_b32_e32 v84, 0
	v_mov_b32_e32 v85, 0
	ds_read_b128 v[194:197], v142
	ds_read_b128 v[198:201], v136
	ds_read_b128 v[202:205], v136 offset:9728
	ds_read_b128 v[206:209], v142 offset:64
	ds_read_b128 v[210:213], v136 offset:64
	ds_read_b128 v[214:217], v136 offset:9792
	ds_read_b128 v[218:221], v142 offset:128
	ds_read_b128 v[222:225], v136 offset:128
	ds_read_b128 v[226:229], v136 offset:9856
	ds_read_b128 v[230:233], v142 offset:192
	ds_read_b128 v[234:237], v136 offset:192
	ds_read_b128 v[238:241], v136 offset:9920
	s_waitcnt lgkmcnt(9)
	v_mfma_f32_16x16x32_f16 v[78:81], v[194:197], v[198:201], v[78:81]
	v_dot2c_f32_f16_e32 v86, v194, v194
	v_dot2c_f32_f16_e32 v86, v195, v195
	v_mfma_f32_16x16x32_f16 v[82:85], v[194:197], v[202:205], v[82:85]
	v_dot2c_f32_f16_e32 v86, v196, v196
	v_dot2c_f32_f16_e32 v86, v197, v197
	ds_read_b128 v[194:197], v142 offset:256
	ds_read_b128 v[198:201], v136 offset:256
	ds_read_b128 v[202:205], v136 offset:9984
	s_waitcnt lgkmcnt(9)
	v_mfma_f32_16x16x32_f16 v[78:81], v[206:209], v[210:213], v[78:81]
	v_dot2c_f32_f16_e32 v86, v206, v206
	v_dot2c_f32_f16_e32 v86, v207, v207
	v_mfma_f32_16x16x32_f16 v[82:85], v[206:209], v[214:217], v[82:85]
	v_dot2c_f32_f16_e32 v86, v208, v208
	v_dot2c_f32_f16_e32 v86, v209, v209
	ds_read_b128 v[206:209], v142 offset:320
	ds_read_b128 v[210:213], v136 offset:320
	ds_read_b128 v[214:217], v136 offset:10048
	s_waitcnt lgkmcnt(9)
	v_mfma_f32_16x16x32_f16 v[78:81], v[218:221], v[222:225], v[78:81]
	v_dot2c_f32_f16_e32 v86, v218, v218
	v_dot2c_f32_f16_e32 v86, v219, v219
	v_mfma_f32_16x16x32_f16 v[82:85], v[218:221], v[226:229], v[82:85]
	v_dot2c_f32_f16_e32 v86, v220, v220
	v_dot2c_f32_f16_e32 v86, v221, v221
	ds_read_b128 v[218:221], v142 offset:384
	ds_read_b128 v[222:225], v136 offset:384
	ds_read_b128 v[226:229], v136 offset:10112
	s_waitcnt lgkmcnt(9)
	v_mfma_f32_16x16x32_f16 v[78:81], v[230:233], v[234:237], v[78:81]
	v_dot2c_f32_f16_e32 v86, v230, v230
	v_dot2c_f32_f16_e32 v86, v231, v231
	v_mfma_f32_16x16x32_f16 v[82:85], v[230:233], v[238:241], v[82:85]
	v_dot2c_f32_f16_e32 v86, v232, v232
	v_dot2c_f32_f16_e32 v86, v233, v233
	ds_read_b128 v[230:233], v142 offset:448
	ds_read_b128 v[234:237], v136 offset:448
	ds_read_b128 v[238:241], v136 offset:10176
	s_waitcnt lgkmcnt(9)
	v_mfma_f32_16x16x32_f16 v[78:81], v[194:197], v[198:201], v[78:81]
	v_dot2c_f32_f16_e32 v86, v194, v194
	v_dot2c_f32_f16_e32 v86, v195, v195
	v_mfma_f32_16x16x32_f16 v[82:85], v[194:197], v[202:205], v[82:85]
	v_dot2c_f32_f16_e32 v86, v196, v196
	v_dot2c_f32_f16_e32 v86, v197, v197
	ds_read_b128 v[194:197], v142 offset:512
	ds_read_b128 v[198:201], v136 offset:512
	ds_read_b128 v[202:205], v136 offset:10240
	s_waitcnt lgkmcnt(9)
	v_mfma_f32_16x16x32_f16 v[78:81], v[206:209], v[210:213], v[78:81]
	v_dot2c_f32_f16_e32 v86, v206, v206
	v_dot2c_f32_f16_e32 v86, v207, v207
	v_mfma_f32_16x16x32_f16 v[82:85], v[206:209], v[214:217], v[82:85]
	v_dot2c_f32_f16_e32 v86, v208, v208
	v_dot2c_f32_f16_e32 v86, v209, v209
	ds_read_b64 v[92:93], v159 offset:20032
	ds_read2st64_b64 v[88:91], v160 offset0:1 offset1:20
	s_waitcnt lgkmcnt(8)
	v_mfma_f32_16x16x32_f16 v[78:81], v[218:221], v[222:225], v[78:81]
	v_dot2c_f32_f16_e32 v86, v218, v218
	v_dot2c_f32_f16_e32 v86, v219, v219
	v_mfma_f32_16x16x32_f16 v[82:85], v[218:221], v[226:229], v[82:85]
	v_dot2c_f32_f16_e32 v86, v220, v220
	v_dot2c_f32_f16_e32 v86, v221, v221
	s_waitcnt lgkmcnt(5)
	v_mfma_f32_16x16x32_f16 v[78:81], v[230:233], v[234:237], v[78:81]
	v_dot2c_f32_f16_e32 v86, v230, v230
	v_dot2c_f32_f16_e32 v86, v231, v231
	v_mfma_f32_16x16x32_f16 v[82:85], v[230:233], v[238:241], v[82:85]
	v_dot2c_f32_f16_e32 v86, v232, v232
	v_dot2c_f32_f16_e32 v86, v233, v233
	s_waitcnt lgkmcnt(2)
	v_mfma_f32_16x16x32_f16 v[78:81], v[194:197], v[198:201], v[78:81]
	v_dot2c_f32_f16_e32 v86, v194, v194
	v_dot2c_f32_f16_e32 v86, v195, v195
	v_mfma_f32_16x16x32_f16 v[82:85], v[194:197], v[202:205], v[82:85]
	v_dot2c_f32_f16_e32 v86, v196, v196
	v_dot2c_f32_f16_e32 v86, v197, v197
	s_waitcnt lgkmcnt(0)
	v_mfma_f32_16x16x16_f16 v[78:81], v[92:93], v[88:89], v[78:81]
	v_dot2c_f32_f16_e32 v86, v92, v92
	v_dot2c_f32_f16_e32 v86, v93, v93
	v_mfma_f32_16x16x16_f16 v[82:85], v[92:93], v[90:91], v[82:85]
	s_nop 1
	v_mov_b32_e32 v87, v86
	s_nop 1
	v_permlane16_swap_b32_e32 v87, v86
	v_add_f32_e32 v86, v86, v87
	v_mov_b32_e32 v87, v86
	s_nop 1
	v_permlane32_swap_b32_e32 v87, v86
	v_add_f32_e32 v86, v86, v87
	v_mul_f32_e32 v87, 0x4f800000, v86
	v_cmp_gt_f32_e32 vcc, s21, v86
	s_nop 1
	v_cndmask_b32_e32 v86, v86, v87, vcc
	v_sqrt_f32_e32 v87, v86
	s_nop 0
	v_add_u32_e32 v88, -1, v87
	v_fma_f32 v90, -v88, v87, v86
	v_add_u32_e32 v89, 1, v87
	v_cmp_ge_f32_e64 s[12:13], 0, v90
	s_nop 1
	v_cndmask_b32_e64 v88, v87, v88, s[12:13]
	v_fma_f32 v87, -v89, v87, v86
	v_cmp_lt_f32_e64 s[12:13], 0, v87
	s_nop 1
	v_cndmask_b32_e64 v87, v88, v89, s[12:13]
	v_mul_f32_e32 v88, 0x37800000, v87
	v_cndmask_b32_e32 v87, v87, v88, vcc
	v_cmp_class_f32_e32 vcc, v86, v135
	s_nop 1
	v_cndmask_b32_e32 v86, v87, v86, vcc
	v_add_f32_e32 v86, 0x29e12e13, v86
	v_div_scale_f32 v87, s[12:13], v86, v86, 1.0
	v_rcp_f32_e32 v88, v87
	v_lshrrev_b32_e32 v89, s3, v191
	v_and_b32_e32 v89, 1, v89
	s_nop 0
	v_fma_f32 v90, -v87, v88, 1.0
	v_fmac_f32_e32 v88, v90, v88
	v_div_scale_f32 v90, vcc, 1.0, v86, 1.0
	v_mul_f32_e32 v91, v90, v88
	v_fma_f32 v92, -v87, v91, v90
	v_fmac_f32_e32 v91, v92, v88
	v_fma_f32 v87, -v87, v91, v90
	v_div_fmas_f32 v87, v87, v88, v91
	v_div_fixup_f32 v86, v87, v86, 1.0
	v_mul_f32_e32 v86, 0x4166d4ca, v86
	v_cmp_eq_u32_e32 vcc, 1, v89
	s_nop 1
	v_cndmask_b32_e32 v86, 0, v86, vcc
	v_cndmask_b32_e64 v87, v161, 0, vcc
	s_and_saveexec_b64 s[24:25], s[4:5]
	ds_write2_b32 v139, v86, v87 offset1:16
	s_or_b64 exec, exec, s[24:25]
	ds_read_b64 v[88:89], v140
	ds_read_b64 v[90:91], v140 offset:64
	s_waitcnt lgkmcnt(0)
	v_mul_f32_e32 v168, v88, v78
	v_mul_f32_e32 v169, v88, v82
	v_pk_mul_f32 v[164:165], v[168:169], s[20:21] op_sel_hi:[1,0]
	v_pk_fma_f32 v[172:173], v[168:169], s[22:23], v[96:97] op_sel_hi:[1,0,0]
	v_pk_fma_f32 v[162:163], v[164:165], v[168:169], v[90:91] op_sel_hi:[1,1,0]
	v_pk_mul_f32 v[164:165], v[172:173], v[172:173] neg_lo:[0,1] neg_hi:[0,1]
	v_exp_f32_e32 v166, v168
	v_exp_f32_e32 v167, v169
	v_exp_f32_e64 v170, -v168
	v_exp_f32_e64 v171, -v169
	v_exp_f32_e32 v162, v162
	v_exp_f32_e32 v164, v164
	v_exp_f32_e32 v165, v165
	v_exp_f32_e32 v163, v163
	v_pk_mul_f32 v[168:169], v[166:167], v[166:167]
	v_pk_mul_f32 v[172:173], v[170:171], v[170:171]
	v_pk_add_f32 v[94:95], v[94:95], v[164:165]
	v_pk_mul_f32 v[164:165], v[166:167], v[162:163]
	v_pk_fma_f32 v[106:107], v[166:167], v[162:163], v[106:107]
	v_pk_mul_f32 v[166:167], v[170:171], v[162:163]
	v_pk_fma_f32 v[108:109], v[170:171], v[162:163], v[108:109]
	v_pk_mul_f32 v[162:163], v[168:169], v[164:165]
	v_pk_fma_f32 v[104:105], v[168:169], v[164:165], v[104:105]
	v_pk_mul_f32 v[164:165], v[172:173], v[166:167]
	v_pk_fma_f32 v[110:111], v[172:173], v[166:167], v[110:111]
	v_pk_mul_f32 v[166:167], v[168:169], v[162:163]
	v_pk_fma_f32 v[102:103], v[168:169], v[162:163], v[102:103]
	v_pk_mul_f32 v[162:163], v[172:173], v[164:165]
	v_pk_fma_f32 v[112:113], v[172:173], v[164:165], v[112:113]
	v_pk_mul_f32 v[164:165], v[168:169], v[166:167]
	v_pk_fma_f32 v[100:101], v[168:169], v[166:167], v[100:101]
	v_pk_mul_f32 v[166:167], v[172:173], v[162:163]
	v_pk_fma_f32 v[114:115], v[172:173], v[162:163], v[114:115]
	v_pk_fma_f32 v[98:99], v[168:169], v[164:165], v[98:99]
	v_pk_fma_f32 v[116:117], v[172:173], v[166:167], v[116:117]
	v_mul_f32_e32 v168, v89, v79
	v_mul_f32_e32 v169, v89, v83
	v_pk_mul_f32 v[164:165], v[168:169], s[20:21] op_sel_hi:[1,0]
	v_pk_fma_f32 v[172:173], v[168:169], s[22:23], v[96:97] op_sel_hi:[1,0,0]
	v_pk_fma_f32 v[162:163], v[164:165], v[168:169], v[90:91] op_sel:[0,0,1] op_sel_hi:[1,1,1]
	v_pk_mul_f32 v[164:165], v[172:173], v[172:173] neg_lo:[0,1] neg_hi:[0,1]
	v_exp_f32_e32 v166, v168
	v_exp_f32_e32 v167, v169
	v_exp_f32_e64 v170, -v168
	v_exp_f32_e64 v171, -v169
	v_exp_f32_e32 v162, v162
	v_exp_f32_e32 v164, v164
	v_exp_f32_e32 v165, v165
	v_exp_f32_e32 v163, v163
	v_pk_mul_f32 v[168:169], v[166:167], v[166:167]
	v_pk_mul_f32 v[172:173], v[170:171], v[170:171]
	v_pk_add_f32 v[94:95], v[94:95], v[164:165]
	v_pk_mul_f32 v[164:165], v[166:167], v[162:163]
	v_pk_fma_f32 v[106:107], v[166:167], v[162:163], v[106:107]
	v_pk_mul_f32 v[166:167], v[170:171], v[162:163]
	v_pk_fma_f32 v[108:109], v[170:171], v[162:163], v[108:109]
	v_pk_mul_f32 v[162:163], v[168:169], v[164:165]
	v_pk_fma_f32 v[104:105], v[168:169], v[164:165], v[104:105]
	v_pk_mul_f32 v[164:165], v[172:173], v[166:167]
	v_pk_fma_f32 v[110:111], v[172:173], v[166:167], v[110:111]
	v_pk_mul_f32 v[166:167], v[168:169], v[162:163]
	v_pk_fma_f32 v[102:103], v[168:169], v[162:163], v[102:103]
	v_pk_mul_f32 v[162:163], v[172:173], v[164:165]
	v_pk_fma_f32 v[112:113], v[172:173], v[164:165], v[112:113]
	v_pk_mul_f32 v[164:165], v[168:169], v[166:167]
	v_pk_fma_f32 v[100:101], v[168:169], v[166:167], v[100:101]
	v_pk_mul_f32 v[166:167], v[172:173], v[162:163]
	v_pk_fma_f32 v[114:115], v[172:173], v[162:163], v[114:115]
	v_pk_fma_f32 v[98:99], v[168:169], v[164:165], v[98:99]
	v_pk_fma_f32 v[116:117], v[172:173], v[166:167], v[116:117]
	s_cmp_eq_u32 s3, 0
	s_cbranch_scc1 .Lret0
	s_cmp_eq_u32 s3, 1
	s_cbranch_scc1 .Lret1
	s_cmp_eq_u32 s3, 2
	s_cbranch_scc1 .Lret2

	.amdhsa_kernel _Z11knrm_kernelPKfS0_PKiS2_S0_Pf
		.amdhsa_group_segment_fixed_size 99712
		.amdhsa_private_segment_fixed_size 0
		.amdhsa_kernarg_size 48
		.amdhsa_user_sgpr_count 2
		.amdhsa_user_sgpr_dispatch_ptr 0
		.amdhsa_user_sgpr_queue_ptr 0
		.amdhsa_user_sgpr_kernarg_segment_ptr 1
		.amdhsa_user_sgpr_dispatch_id 0
		.amdhsa_user_sgpr_kernarg_preload_length 0
		.amdhsa_user_sgpr_kernarg_preload_offset 0
		.amdhsa_user_sgpr_private_segment_size 0
		.amdhsa_uses_dynamic_stack 0
		.amdhsa_enable_private_segment 0
		.amdhsa_system_sgpr_workgroup_id_x 1
		.amdhsa_system_sgpr_workgroup_id_y 0
		.amdhsa_system_sgpr_workgroup_id_z 0
		.amdhsa_system_sgpr_workgroup_info 0
		.amdhsa_system_vgpr_workitem_id 0
		.amdhsa_next_free_vgpr 242
		.amdhsa_next_free_sgpr 96
		.amdhsa_accum_offset 244
		.amdhsa_reserve_vcc 1
		.amdhsa_float_round_mode_32 0
		.amdhsa_float_round_mode_16_64 0
		.amdhsa_float_denorm_mode_32 3
		.amdhsa_float_denorm_mode_16_64 3
		.amdhsa_dx10_clamp 1
		.amdhsa_ieee_mode 1
		.amdhsa_fp16_overflow 0
		.amdhsa_tg_split 0
		.amdhsa_exception_fp_ieee_invalid_op 0
		.amdhsa_exception_fp_denorm_src 0
		.amdhsa_exception_fp_ieee_div_zero 0
		.amdhsa_exception_fp_ieee_overflow 0
		.amdhsa_exception_fp_ieee_underflow 0
		.amdhsa_exception_fp_ieee_inexact 0
		.amdhsa_exception_int_div_zero 0
	.end_amdhsa_kernel

amdhsa.kernels:
  - .agpr_count:     0
    .args:
      - .actual_access:  read_only
        .address_space:  global
        .offset:         0
        .size:           8
        .value_kind:     global_buffer
      - .actual_access:  read_only
        .address_space:  global
        .offset:         8
        .size:           8
        .value_kind:     global_buffer
      - .actual_access:  read_only
        .address_space:  global
        .offset:         16
        .size:           8
        .value_kind:     global_buffer
      - .actual_access:  read_only
        .address_space:  global
        .offset:         24
        .size:           8
        .value_kind:     global_buffer
      - .actual_access:  read_only
        .address_space:  global
        .offset:         32
        .size:           8
        .value_kind:     global_buffer
      - .actual_access:  write_only
        .address_space:  global
        .offset:         40
        .size:           8
        .value_kind:     global_buffer
    .group_segment_fixed_size: 99712
    .kernarg_segment_align: 8
    .kernarg_segment_size: 48
    .language:       OpenCL C
    .language_version:
      - 2
      - 0
    .max_flat_workgroup_size: 512
    .name:           _Z11knrm_kernelPKfS0_PKiS2_S0_Pf
    .private_segment_fixed_size: 0
    .sgpr_count:     32
    .sgpr_spill_count: 0
    .symbol:         _Z11knrm_kernelPKfS0_PKiS2_S0_Pf.kd
    .uniform_work_group_size: 1
    .uses_dynamic_stack: false
    .vgpr_count:     242
    .vgpr_spill_count: 0
    .wavefront_size: 64
